# prologue de-serialisation, dilated attention units: queue pre-claim atomic, bias-table load and first K/V DMA overlap (one round trip instead of three); set-up barrier merged into DMA prologue barrier
# baseline (speedup 1.0000x reference)
.LBB0_1514:
	s_cmpk_lt_i32 s30, 0x500
	s_cselect_b64 s[30:31], -1, 0
	s_cmp_lt_i32 s33, 2
	s_mov_b64 s[12:13], -1
	s_cbranch_scc1 .LBB0_1615
	s_cmp_gt_i32 s33, 2
	s_cbranch_scc0 .LBB0_1603
	v_mov_b32_e32 v4, v233
	v_mov_b32_e32 v7, 0
	v_cmp_eq_u32_e32 vcc, 0, v4
	v_readfirstlane_b32 s41, v4
	s_and_b64 s[12:13], s[30:31], vcc
	s_and_saveexec_b64 s[34:35], s[12:13]
	s_cbranch_execz .LBB0_1520
	s_mov_b64 s[38:39], exec
	v_mbcnt_lo_u32_b32 v2, s38, 0
	v_mbcnt_hi_u32_b32 v2, s39, v2
	v_cmp_eq_u32_e32 vcc, 0, v2
	s_and_saveexec_b64 s[36:37], vcc
	s_cbranch_execz .LBB0_1519
	s_bcnt1_i32_b64 s38, s[38:39]
	v_mov_b32_e32 v102, s38
	global_atomic_add v102, v3, v102, s[14:15] sc0

.LBB0_1520:
	s_or_b64 exec, exec, s[34:35]
	s_ashr_i32 s50, s41, 6
	s_lshl_b32 s51, s82, 8
	s_lshl_b32 s46, s50, 5
	s_lshl_b32 s36, s83, 11
	s_add_i32 s46, s46, s51
	s_and_b64 s[34:35], s[4:5], exec
	s_movk_i32 s34, 0x80
	s_cselect_b32 s37, 0x200, s34
	s_and_b64 s[34:35], s[10:11], exec
	v_and_b32_e32 v138, 31, v4
	s_cselect_b32 s47, 0x800, s37
	s_and_b64 s[4:5], s[4:5], exec
	v_or_b32_e32 v136, s46, v138
	s_cselect_b32 s34, 2, 4
	s_and_b64 s[4:5], s[10:11], exec
	v_cmp_gt_i32_e32 vcc, s47, v136
	s_cselect_b32 s45, 0, s34
	s_lshl_b32 s4, s40, 23
	v_cndmask_b32_e32 v2, 0, v136, vcc
	s_add_u32 s4, s16, s4
	v_lshlrev_b32_e32 v2, s45, v2
	s_addc_u32 s5, s17, 0
	s_or_b32 s35, s36, s7
	v_add_u32_e32 v8, s35, v2
	v_ashrrev_i32_e32 v9, 31, v8
	v_lshlrev_b64 v[8:9], 9, v[8:9]
	v_bfe_u32 v6, v4, 5, 1
	v_lshl_add_u64 v[8:9], s[4:5], 0, v[8:9]
	s_lshl_b32 s48, s6, 7
	v_lshl_add_u64 v[8:9], v[8:9], 0, s[48:49]
	v_lshlrev_b32_e32 v2, 4, v6
	v_lshl_add_u64 v[8:9], v[8:9], 0, v[2:3]
	s_mov_b64 s[10:11], 0x4000000
	v_lshl_add_u64 v[132:133], v[8:9], 0, s[10:11]
	v_add_co_u32_e32 v8, vcc, 0x4000000, v8
	s_movk_i32 s10, 0x100
	s_nop 0
	v_addc_co_u32_e32 v9, vcc, 0, v9, vcc
	global_load_dwordx4 v[116:119], v[132:133], off offset:32
	global_load_dwordx4 v[120:123], v[132:133], off offset:64
	global_load_dwordx4 v[124:127], v[8:9], off
	global_load_dwordx4 v[128:131], v[132:133], off offset:96
	s_lshl_b32 s34, s40, 2
	v_cmp_gt_i32_e32 vcc, s10, v4
	s_and_saveexec_b64 s[10:11], vcc
	s_cbranch_execz .LBB0_1524
	v_cmp_lt_i32_e32 vcc, 63, v4
	v_mov_b32_e32 v100, 0xf149f2ca
	s_nop 0
	s_and_saveexec_b64 s[38:39], vcc
	s_cbranch_execz .LBB0_1523
	s_or_b32 s37, s34, s6
	s_mul_i32 s48, s37, 0xc0
	s_lshl_b64 s[40:41], s[48:49], 2
	s_add_u32 s40, s0, s40
	s_addc_u32 s41, s1, s41
	v_mov_b32_e32 v5, v3
	v_lshl_add_u64 v[8:9], v[4:5], 2, s[40:41]
	v_add_co_u32_e32 v8, vcc, 0x129000, v8
	s_nop 1
	v_addc_co_u32_e32 v9, vcc, 0, v9, vcc
	global_load_dword v100, v[8:9], off offset:768

.LBB0_1524:
	s_or_b64 exec, exec, s[10:11]
	s_waitcnt lgkmcnt(0)
	v_and_b32_e32 v137, 63, v4
	s_lshl_b32 s38, s6, 6
	s_ashr_i32 s37, s36, 31
	s_lshl_b64 s[10:11], s[36:37], 9
	s_add_u32 s4, s4, s10
	s_addc_u32 s5, s5, s11
	s_lshl_b32 s10, s38, 1
	s_add_u32 s4, s4, s10
	s_addc_u32 s5, s5, 0
	s_add_u32 s10, s4, 0x7000000
	s_addc_u32 s11, s5, 0
	s_add_i32 s48, s51, 0xffffff80
	s_add_u32 s4, s4, 0x5800000
	s_addc_u32 s5, s5, 0
	s_cmp_eq_u32 s82, 0
	s_cselect_b32 s61, 2, 0
	s_or_b32 s59, s61, 1
	s_add_i32 s52, s61, 2
	s_cmp_le_u32 s52, s44
	s_cselect_b64 s[40:41], -1, 0
	s_add_i32 s12, s61, 3
	s_cmp_gt_u32 s52, s44
	s_cselect_b32 s53, s52, s12
	s_lshl_b32 s38, s61, 6
	s_add_i32 s57, s38, s48
	v_or_b32_e32 v2, s57, v137
	v_max_i32_e32 v2, 0, v2
	v_lshlrev_b32_e32 v2, s45, v2
	v_add_u32_e32 v4, s7, v2
	v_ashrrev_i32_e32 v5, 31, v4
	s_lshl_b32 s36, s50, 3
	v_lshlrev_b64 v[4:5], 9, v[4:5]
	s_ashr_i32 s37, s36, 31
	v_lshl_add_u64 v[4:5], s[4:5], 0, v[4:5]
	s_lshl_b64 s[12:13], s[36:37], 1
	s_lshl_b32 s58, s50, 10
	v_lshl_add_u64 v[4:5], v[4:5], 0, s[12:13]
	s_add_i32 s54, s58, s68
	s_mov_b32 s39, m0
	s_mov_b32 m0, s54
	s_nop 0
	global_load_lds_dwordx4 v[4:5], off
	s_mov_b32 m0, s39
	s_lshl_b32 s39, s59, 6
	s_add_i32 s60, s39, s48
	v_or_b32_e32 v2, s60, v137
	v_max_i32_e32 v2, 0, v2
	v_lshlrev_b32_e32 v2, s45, v2
	v_add_u32_e32 v4, s7, v2
	v_ashrrev_i32_e32 v5, 31, v4
	v_lshlrev_b64 v[4:5], 9, v[4:5]
	v_lshl_add_u64 v[4:5], s[4:5], 0, v[4:5]
	v_lshl_add_u64 v[4:5], v[4:5], 0, s[12:13]
	s_add_i32 s39, s58, s71
	v_lshrrev_b32_e32 v7, 2, v137
	s_mov_b32 s42, m0
	s_mov_b32 m0, s39
	s_nop 0
	global_load_lds_dwordx4 v[4:5], off
	s_mov_b32 m0, s42
	s_lshl_b32 s39, s50, 4
	v_or_b32_e32 v4, s48, v7
	s_and_b32 s56, s39, 48
	v_add_u32_e32 v2, s38, v4
	v_or_b32_e32 v2, s56, v2
	v_max_i32_e32 v2, 0, v2
	v_lshlrev_b32_e32 v2, s45, v2
	v_add_u32_e32 v8, s7, v2
	v_ashrrev_i32_e32 v9, 31, v8
	v_lshlrev_b64 v[8:9], 9, v[8:9]
	s_and_b32 s38, s36, 0xffffffe0
	v_lshlrev_b32_e32 v2, 3, v137
	v_lshl_add_u64 v[8:9], s[10:11], 0, v[8:9]
	s_ashr_i32 s39, s38, 31
	v_and_b32_e32 v5, 24, v2
	v_lshl_add_u64 v[8:9], s[38:39], 1, v[8:9]
	v_lshlrev_b32_e32 v2, 1, v5
	v_lshl_add_u64 v[8:9], v[8:9], 0, v[2:3]
	s_add_i32 s55, s58, s72
	s_mov_b32 s42, m0
	s_mov_b32 m0, s55
	s_nop 0
	global_load_lds_dwordx4 v[8:9], off
	s_mov_b32 m0, s42
	v_or_b32_e32 v7, s60, v7
	s_mov_b64 s[42:43], -1
	s_cmp_gt_u32 s53, s44
	v_or_b32_e32 v7, s56, v7
	s_cbranch_scc1 .LBB0_1528
	s_lshl_b32 s60, s52, 6
	s_add_i32 s42, s60, s48
	v_or_b32_e32 v8, s42, v137
	v_lshlrev_b32_e32 v8, s45, v8
	v_add_u32_e32 v8, s7, v8
	v_ashrrev_i32_e32 v9, 31, v8
	v_lshlrev_b64 v[8:9], 9, v[8:9]
	v_lshl_add_u64 v[8:9], s[4:5], 0, v[8:9]
	v_lshl_add_u64 v[8:9], v[8:9], 0, s[12:13]
	s_add_i32 s42, s58, s73
	s_mov_b32 s43, m0
	s_mov_b32 m0, s42
	s_nop 0
	global_load_lds_dwordx4 v[8:9], off
	s_mov_b32 m0, s43
	v_max_i32_e32 v8, 0, v7
	v_lshlrev_b32_e32 v8, s45, v8
	v_add_u32_e32 v8, s7, v8
	v_ashrrev_i32_e32 v9, 31, v8
	v_lshlrev_b64 v[8:9], 9, v[8:9]
	v_lshl_add_u64 v[8:9], s[10:11], 0, v[8:9]
	s_lshl_b64 s[42:43], s[38:39], 1
	v_lshl_add_u64 v[8:9], v[8:9], 0, s[42:43]
	s_add_i32 s62, s58, s76
	v_lshl_add_u64 v[8:9], v[8:9], 0, v[2:3]
	s_mov_b32 s63, m0
	s_mov_b32 m0, s62
	s_nop 0
	global_load_lds_dwordx4 v[8:9], off
	s_mov_b32 m0, s63
	s_lshl_b32 s62, s53, 6
	s_add_i32 s62, s62, s48
	v_or_b32_e32 v8, s62, v137
	v_lshlrev_b32_e32 v8, s45, v8
	v_add_u32_e32 v8, s7, v8
	v_ashrrev_i32_e32 v9, 31, v8
	v_lshlrev_b64 v[8:9], 9, v[8:9]
	v_lshl_add_u64 v[8:9], s[4:5], 0, v[8:9]
	v_lshl_add_u64 v[8:9], v[8:9], 0, s[12:13]
	s_add_i32 s62, s58, s77
	s_mov_b32 s63, m0
	s_mov_b32 m0, s62
	s_nop 0
	global_load_lds_dwordx4 v[8:9], off
	s_mov_b32 m0, s63
	v_add_u32_e32 v8, s60, v4
	v_or_b32_e32 v8, s56, v8
	v_max_i32_e32 v8, 0, v8
	v_lshlrev_b32_e32 v8, s45, v8
	v_add_u32_e32 v8, s7, v8
	v_ashrrev_i32_e32 v9, 31, v8
	v_lshlrev_b64 v[8:9], 9, v[8:9]
	v_lshl_add_u64 v[8:9], s[10:11], 0, v[8:9]
	v_lshl_add_u64 v[8:9], v[8:9], 0, s[42:43]
	v_lshl_add_u64 v[8:9], v[8:9], 0, v[2:3]
	s_add_i32 s42, s58, s78
	s_mov_b32 s43, m0
	s_mov_b32 m0, s42
	s_nop 0
	global_load_lds_dwordx4 v[8:9], off
	s_mov_b32 m0, s43
	s_waitcnt vmcnt(7)
	v_cmp_gt_u32_e32 vcc, 0x100, v233
	s_and_saveexec_b64 s[36:37], vcc
	v_lshl_add_u32 v101, v233, 2, s70
	ds_write_b32 v101, v100
	s_mov_b64 exec, s[36:37]
	v_cmp_eq_u32_e32 vcc, 0, v233
	s_and_b64 vcc, s[30:31], vcc
	s_and_saveexec_b64 s[36:37], vcc
	v_mov_b32_e32 v101, s69
	ds_write_b32 v101, v102
	s_mov_b64 exec, s[36:37]
	s_waitcnt vmcnt(4) lgkmcnt(0)
	s_barrier
	s_mov_b64 s[42:43], 0

.LBB0_1533:
	s_waitcnt vmcnt(0)
	v_cmp_gt_u32_e32 vcc, 0x100, v233
	s_and_saveexec_b64 s[36:37], vcc
	v_lshl_add_u32 v101, v233, 2, s70
	ds_write_b32 v101, v100
	s_mov_b64 exec, s[36:37]
	v_cmp_eq_u32_e32 vcc, 0, v233
	s_and_b64 vcc, s[30:31], vcc
	s_and_saveexec_b64 s[36:37], vcc
	v_mov_b32_e32 v101, s69
	ds_write_b32 v101, v102
	s_mov_b64 exec, s[36:37]
	s_waitcnt vmcnt(0) lgkmcnt(0)
	s_barrier
